# attention step loops (7.12): branch straight to the barrier after the selected counted vmcnt wait instead of falling through the remaining ladder levels; on top of the accumulator no-copy version
# speedup vs baseline: 1.0111x; 1.0074x over previous
.LBB0_679:
	v_add_co_u32_e64 v66, s[80:81], s87, 1
	s_nop 0
	v_readfirstlane_b32 s68, v66
	s_min_u32 s68, s68, 3
	s_lshl_b32 s68, s68, 1
	s_cmp_gt_i32 s73, 63
	s_cselect_b64 s[84:85], -1, 0
	s_and_b64 vcc, s[84:85], exec
	s_cselect_b32 s79, 8, 16
	s_min_i32 vcc_lo, s87, 2
	s_lshl_b32 vcc_lo, vcc_lo, 1
	s_add_i32 vcc_lo, vcc_lo, 8
	s_and_b64 s[80:81], s[80:81], exec
	s_cselect_b32 s80, 8, vcc_lo
	s_and_b32 s81, s78, -2
	s_or_b32 s79, s68, s79
	s_cmp_eq_u32 s78, 4
	s_cselect_b32 s68, s80, s68
	s_cmp_eq_u32 s81, 2
	s_cselect_b32 s68, s79, s68
	s_cmp_lt_u32 s68, 22
	s_mov_b64 s[80:81], -1
	s_cbranch_scc0 .LBB0_721
	s_cmp_lt_u32 s68, 20
	s_cbranch_scc0 .LBB0_718
	s_cmp_lt_u32 s68, 18
	s_cbranch_scc0 .LBB0_715
	s_cmp_lt_u32 s68, 16
	s_cbranch_scc0 .LBB0_712
	s_cmp_lt_u32 s68, 14
	s_cbranch_scc0 .LBB0_709
	s_cmp_lt_u32 s68, 12
	s_cbranch_scc0 .LBB0_706
	s_cmp_lt_u32 s68, 10
	s_cbranch_scc0 .LBB0_703
	s_cmp_lt_u32 s68, 8
	s_cbranch_scc0 .LBB0_700
	s_cmp_lt_u32 s68, 6
	s_cbranch_scc0 .LBB0_697
	s_cmp_lt_u32 s68, 4
	s_cbranch_scc0 .LBB0_694
	s_cmp_eq_u32 s68, 0
	s_cbranch_scc1 .LBB0_691
	s_waitcnt vmcnt(2)
	s_branch .LBB0_723
	s_mov_b64 s[80:81], 0
.LBB0_691:
	s_andn2_b64 vcc, exec, s[80:81]
	s_cbranch_vccnz .LBB0_693
	s_waitcnt vmcnt(0)
	s_branch .LBB0_723

.LBB0_694:
	s_andn2_b64 vcc, exec, s[80:81]
	s_cbranch_vccnz .LBB0_696
	s_waitcnt vmcnt(4)
	s_branch .LBB0_723

.LBB0_697:
	s_andn2_b64 vcc, exec, s[80:81]
	s_cbranch_vccnz .LBB0_699
	s_waitcnt vmcnt(6)
	s_branch .LBB0_723

.LBB0_700:
	s_andn2_b64 vcc, exec, s[80:81]
	s_cbranch_vccnz .LBB0_702
	s_waitcnt vmcnt(8)
	s_branch .LBB0_723

.LBB0_703:
	s_andn2_b64 vcc, exec, s[80:81]
	s_cbranch_vccnz .LBB0_705
	s_waitcnt vmcnt(10)
	s_branch .LBB0_723

.LBB0_706:
	s_andn2_b64 vcc, exec, s[80:81]
	s_cbranch_vccnz .LBB0_708
	s_waitcnt vmcnt(12)
	s_branch .LBB0_723

.LBB0_709:
	s_andn2_b64 vcc, exec, s[80:81]
	s_cbranch_vccnz .LBB0_711
	s_waitcnt vmcnt(14)
	s_branch .LBB0_723

.LBB0_712:
	s_andn2_b64 vcc, exec, s[80:81]
	s_cbranch_vccnz .LBB0_714
	s_waitcnt vmcnt(16)
	s_branch .LBB0_723

.LBB0_715:
	s_andn2_b64 vcc, exec, s[80:81]
	s_cbranch_vccnz .LBB0_717
	s_waitcnt vmcnt(18)
	s_branch .LBB0_723

.LBB0_718:
	s_andn2_b64 vcc, exec, s[80:81]
	s_cbranch_vccnz .LBB0_720
	s_waitcnt vmcnt(20)
	s_branch .LBB0_723

.LBB0_749:
	v_add_co_u32_e64 v66, s[80:81], s72, 1
	s_nop 0
	v_readfirstlane_b32 s68, v66
	s_min_u32 s68, s68, 3
	s_lshl_b32 s68, s68, 1
	s_cmp_gt_i32 s73, 63
	s_cselect_b64 s[84:85], -1, 0
	s_and_b64 vcc, s[84:85], exec
	s_cselect_b32 s79, 8, 16
	s_min_i32 vcc_lo, s72, 2
	s_lshl_b32 vcc_lo, vcc_lo, 1
	s_add_i32 vcc_lo, vcc_lo, 8
	s_and_b64 s[80:81], s[80:81], exec
	s_cselect_b32 s80, 8, vcc_lo
	s_and_b32 s81, s78, -2
	s_or_b32 s79, s68, s79
	s_cmp_eq_u32 s78, 4
	s_cselect_b32 s68, s80, s68
	s_cmp_eq_u32 s81, 2
	s_cselect_b32 s68, s79, s68
	s_cmp_lt_u32 s68, 22
	s_mov_b64 s[80:81], -1
	s_cbranch_scc0 .LBB0_791
	s_cmp_lt_u32 s68, 20
	s_cbranch_scc0 .LBB0_788
	s_cmp_lt_u32 s68, 18
	s_cbranch_scc0 .LBB0_785
	s_cmp_lt_u32 s68, 16
	s_cbranch_scc0 .LBB0_782
	s_cmp_lt_u32 s68, 14
	s_cbranch_scc0 .LBB0_779
	s_cmp_lt_u32 s68, 12
	s_cbranch_scc0 .LBB0_776
	s_cmp_lt_u32 s68, 10
	s_cbranch_scc0 .LBB0_773
	s_cmp_lt_u32 s68, 8
	s_cbranch_scc0 .LBB0_770
	s_cmp_lt_u32 s68, 6
	s_cbranch_scc0 .LBB0_767
	s_cmp_lt_u32 s68, 4
	s_cbranch_scc0 .LBB0_764
	s_cmp_eq_u32 s68, 0
	s_cbranch_scc1 .LBB0_761
	s_waitcnt vmcnt(2)
	s_branch .LBB0_793
	s_mov_b64 s[80:81], 0

.LBB0_819:
	s_add_i32 s78, s87, 1
	s_min_u32 s78, s78, 3
	s_lshl_b32 s78, s78, 1
	s_cmp_gt_i32 s68, 63
	s_cselect_b64 s[84:85], -1, 0
	s_and_b64 s[80:81], s[84:85], exec
	s_cselect_b32 s80, 8, 16
	s_min_i32 s81, s87, 2
	s_lshl_b32 s81, s81, 1
	s_add_i32 s81, s81, 8
	s_cmp_lg_u32 s73, 63
	s_cselect_b32 s81, s81, 8
	s_and_b32 vcc_lo, s79, -2
	s_or_b32 s80, s78, s80
	s_cmp_eq_u32 s79, 4
	s_cselect_b32 s78, s81, s78
	s_cmp_eq_u32 vcc_lo, 2
	s_cselect_b32 s78, s80, s78
	s_cmp_lt_u32 s78, 22
	s_mov_b64 s[80:81], -1
	s_cbranch_scc0 .LBB0_861
	s_cmp_lt_u32 s78, 20
	s_cbranch_scc0 .LBB0_858
	s_cmp_lt_u32 s78, 18
	s_cbranch_scc0 .LBB0_855
	s_cmp_lt_u32 s78, 16
	s_cbranch_scc0 .LBB0_852
	s_cmp_lt_u32 s78, 14
	s_cbranch_scc0 .LBB0_849
	s_cmp_lt_u32 s78, 12
	s_cbranch_scc0 .LBB0_846
	s_cmp_lt_u32 s78, 10
	s_cbranch_scc0 .LBB0_843
	s_cmp_lt_u32 s78, 8
	s_cbranch_scc0 .LBB0_840
	s_cmp_lt_u32 s78, 6
	s_cbranch_scc0 .LBB0_837
	s_cmp_lt_u32 s78, 4
	s_cbranch_scc0 .LBB0_834
	s_cmp_eq_u32 s78, 0
	s_cbranch_scc1 .LBB0_831
	s_waitcnt vmcnt(2)
	s_branch .LBB0_863
	s_mov_b64 s[80:81], 0
